# diff attention: second barrier before PV, waves 4-7 run half a tile behind (QK/softmax beside PV)
# baseline (speedup 1.0000x reference)
; #define LAS __attribute__((address_space(3)))
; __device__ __forceinline__ int opaque_tid() { int t = threadIdx.x; asm volatile("" : "+v"(t)); return t; }
; __device__ __forceinline__ void diff_unit(int u, const f16* Z, f16* Y, const float* subln, float lam, LAS unsigned char* lds) {
;     const int tid = opaque_tid(), lane = tid & 63, wave = __builtin_amdgcn_readfirstlane(tid >> 6);
;     const int qb = u & 15, h = (u >> 4) & 3, b = u >> 6;
;     const int map = wave >> 2, r32 = lane & 31, hh = lane >> 5;
; template <class Hook>
; __device__ __forceinline__ void attn_phase(const f16* Z, f16* Y, const float* rpb, const float* subln, const float* lamp, LAS unsigned char* lds, int rep, Hook& HK) {
;     const float lam = *lamp;
;     const int ulo = (rep == 3) ? 1024 : 0, uhi = (rep == 2) ? 1024 : 2048;
;     for (int u = ulo + blockIdx.x; u < uhi; u += gridDim.x) {
;         if (u < 1024) diff_unit(u, Z, Y, subln, lam, lds);
;         else na_unit(u - 1024, Z, Y, rpb, lds);
.LBB0_479:
	v_readfirstlane_b32 s98, v0
	s_nop 3
	s_lshr_b32 s98, s98, 8
	s_cmp_lt_i32 s80, 4
	s_cselect_b64 s[0:1], -1, 0
	s_add_u32 s4, s90, 0x33e00000
	s_addc_u32 s5, s91, 0
	s_add_u32 s84, s90, 0x1600000
	s_addc_u32 s85, s91, 0
	v_writelane_b32 v250, s4, 14
	s_add_u32 s78, s90, 0xc600000
	s_nop 0
	v_writelane_b32 v250, s5, 15
	s_addc_u32 s4, s91, 0
	s_and_b64 s[56:57], s[0:1], s[2:3]
	s_mov_b64 s[0:1], s[80:81]
	v_writelane_b32 v250, s4, 16
	s_mov_b32 s2, s82
	v_writelane_b32 v250, s0, 17
	s_andn2_b64 vcc, exec, s[56:57]
	s_nop 0
	v_writelane_b32 v250, s1, 18
	v_writelane_b32 v250, s2, 19
	v_writelane_b32 v250, s3, 20
	v_writelane_b32 v250, s62, 21
	s_nop 1
	v_writelane_b32 v250, s63, 22
	v_writelane_b32 v250, s76, 23
	s_nop 1
	v_writelane_b32 v250, s77, 24
	v_writelane_b32 v250, s84, 25
	v_writelane_b32 v250, s85, 26
	s_cbranch_vccnz .LBB0_641
	s_cmp_eq_u32 s82, 3
	s_cselect_b32 s0, 0x400, 0
	s_cmp_eq_u32 s82, 2
	s_movk_i32 s1, 0x800
	s_cselect_b32 s1, 0x400, s1
	s_add_i32 s33, s0, s92
	s_cmp_lt_i32 s33, s1
	v_writelane_b32 v250, s1, 27
	s_cbranch_scc1 .LBB0_482
	s_mul_i32 s20, s92, 0x1080
	s_add_i32 s0, s92, 1
	s_mul_hi_u32 s21, s92, 0x1080
	s_mul_hi_u32 s23, s0, 0x1080
	s_add_i32 s22, s20, 0x1080
	s_mov_b64 s[0:1], -1
	s_cbranch_execz .LBB0_483
	s_branch .LBB0_611

; #define LAS __attribute__((address_space(3)))
; __device__ __forceinline__ int fsw(int row) { return ((row & 3) << 2) | ((row >> 2) & 3); }
; __device__ __forceinline__ void dma_tile(const f16* Z, long rowbase, int kcol, int vcol, LAS unsigned char* slot, int wave, int lane) {
;     const unsigned sbase = (unsigned)__builtin_amdgcn_readfirstlane((int)(unsigned)(uintptr_t)slot);
; #pragma unroll
;     for (int i = 0; i < 2; ++i) { const int piece = wave + 8 * i, row = 4 * piece + (lane >> 4), c = (lane & 15) ^ fsw(row);
;         const f16* gp = Z + (size_t)(rowbase + row) * ZP0 + 8 * c;
;         glds16(gp + kcol, sbase + piece * 1024);
;         glds16(gp + vcol, sbase + 16384 + piece * 1024); }
; }
; __device__ __forceinline__ void diff_unit(int u, const f16* Z, f16* Y, const float* subln, float lam, LAS unsigned char* lds) {
;     ...
;     const long tokbase = (long)b * SEQ;
;     const long qrow = tokbase + qb * 128 + (wave & 3) * 32 + r32;
;     const int kcol = 1536 + 128 * h, vcol = 2560 + 128 * h;
;     constexpr int NT = 36;
;     ...
; #pragma unroll
;     for (int t = 0; t < 3; ++t) dma_tile(Z, DIFF_ROWBASE(t), kcol, vcol, lds + t * SLOT, wave, lane);
.LBB0_547:
	s_and_b64 vcc, exec, s[0:1]
	s_cbranch_vccz .LBB0_577
	v_mov_b32_e32 v8, v0
	s_ashr_i32 s2, s33, 6
	v_readfirstlane_b32 s11, v8
	s_ashr_i32 s4, s11, 6
	s_ashr_i32 s3, s2, 31
	v_bfe_u32 v4, v8, 4, 2
	s_lshl_b64 s[0:1], s[2:3], 11
	s_lshl_b32 s3, s33, 7
	s_and_b32 s12, s4, 3
	v_and_b32_e32 v2, 15, v8
	v_lshlrev_b32_e32 v5, 2, v4
	s_and_b32 s3, s3, 0x780
	s_lshl_b32 s5, s12, 5
	v_bitop3_b32 v2, v5, v2, s12 bitop3:0x36
	v_lshl_or_b32 v206, s4, 2, v4
	s_or_b32 s3, s5, s3
	v_lshlrev_b32_e32 v2, 4, v2
	v_ashrrev_i32_e32 v207, 31, v206
	s_lshl_b32 s13, s4, 10
	s_add_i32 s4, s4, 8
	v_and_or_b32 v9, v8, 31, s3
	s_lshl_b32 s3, s33, 3
	v_lshl_add_u64 v[204:205], s[76:77], 0, v[2:3]
	v_lshl_or_b32 v208, s4, 2, v4
	v_lshl_add_u64 v[4:5], s[0:1], 0, v[206:207]
	s_and_b32 s10, s3, 0x180
	s_lshl_b32 s14, s4, 10
	v_mad_u64_u32 v[6:7], s[4:5], v4, s71, v[204:205]
	v_mad_i32_i24 v7, v5, s71, v7
	s_lshl_b32 s86, s10, 1
	v_lshl_add_u64 v[4:5], v[6:7], 0, s[86:87]
	s_mov_b64 s[18:19], 0xc00
	s_or_b32 s3, s10, 0xa00
	v_lshl_add_u64 v[4:5], v[4:5], 0, s[18:19]
	s_add_i32 s4, s13, 0
	s_mov_b32 s5, m0
	s_mov_b32 m0, s4
	s_nop 0
	global_load_lds_dwordx4 v[4:5], off
	s_mov_b32 m0, s5
	s_lshl_b32 s4, s3, 1
	s_mov_b32 s5, s87
	v_ashrrev_i32_e32 v209, 31, v208
	v_lshl_add_u64 v[4:5], v[6:7], 0, s[4:5]
	s_add_i32 s8, 0, 0x4000
	s_add_i32 s6, s13, s8
	s_mov_b32 s7, m0
	s_mov_b32 m0, s6
	s_nop 0
	global_load_lds_dwordx4 v[4:5], off
	s_mov_b32 m0, s7
	v_lshl_add_u64 v[4:5], s[0:1], 0, v[208:209]
	v_mad_u64_u32 v[6:7], s[6:7], v4, s71, v[204:205]
	v_mad_i32_i24 v7, v5, s71, v7
	v_lshl_add_u64 v[4:5], v[6:7], 0, s[86:87]
	v_lshl_add_u64 v[4:5], v[4:5], 0, s[18:19]
	s_add_i32 s6, s14, 0
	s_mov_b32 s7, m0
	s_mov_b32 m0, s6
	s_nop 0
	global_load_lds_dwordx4 v[4:5], off
	s_mov_b32 m0, s7
	v_lshl_add_u64 v[4:5], v[6:7], 0, s[4:5]
	s_add_i32 s6, s14, s8
	s_mov_b32 s7, m0
	s_mov_b32 m0, s6
	s_nop 0
	global_load_lds_dwordx4 v[4:5], off
	s_mov_b32 m0, s7
	s_or_b32 s6, s0, 64
	s_mov_b32 s7, s1
	v_lshl_add_u64 v[4:5], s[6:7], 0, v[206:207]
	v_mad_u64_u32 v[6:7], s[8:9], v4, s71, v[204:205]
	v_mad_i32_i24 v7, v5, s71, v7
	v_lshl_add_u64 v[4:5], v[6:7], 0, s[86:87]
	v_lshl_add_u64 v[4:5], v[4:5], 0, s[18:19]
	s_add_i32 s8, 0, 0x8000
	s_add_i32 s9, s13, s8
	s_mov_b32 s15, m0
	s_mov_b32 m0, s9
	s_nop 0
	global_load_lds_dwordx4 v[4:5], off
	s_mov_b32 m0, s15
	v_lshl_add_u64 v[4:5], v[6:7], 0, s[4:5]
	v_readlane_b32 s16, v250, 41
	s_add_i32 s9, s13, s16
	s_mov_b32 s15, m0
	s_mov_b32 m0, s9
	s_nop 0
	global_load_lds_dwordx4 v[4:5], off
	s_mov_b32 m0, s15
	v_lshl_add_u64 v[4:5], s[6:7], 0, v[208:209]
	v_mad_u64_u32 v[6:7], s[6:7], v4, s71, v[204:205]
	v_mad_i32_i24 v7, v5, s71, v7
	v_lshl_add_u64 v[4:5], v[6:7], 0, s[86:87]
	v_lshl_add_u64 v[4:5], v[4:5], 0, s[18:19]
	s_add_i32 s6, s14, s8
	s_mov_b32 s7, m0
	s_mov_b32 m0, s6
	s_nop 0
	global_load_lds_dwordx4 v[4:5], off
	s_mov_b32 m0, s7
	v_lshl_add_u64 v[4:5], v[6:7], 0, s[4:5]
	s_add_i32 s6, s14, s16
	s_mov_b32 s7, m0
	s_mov_b32 m0, s6
	s_nop 0
	global_load_lds_dwordx4 v[4:5], off
	s_mov_b32 m0, s7
	s_or_b32 s6, s0, 0x80
	s_mov_b32 s7, s1
	v_lshl_add_u64 v[4:5], s[6:7], 0, v[206:207]
	v_mad_u64_u32 v[6:7], s[8:9], v4, s71, v[204:205]
	v_mad_i32_i24 v7, v5, s71, v7
	v_lshl_add_u64 v[4:5], v[6:7], 0, s[86:87]
	v_lshl_add_u64 v[4:5], v[4:5], 0, s[18:19]
	v_readlane_b32 s15, v250, 42
	s_add_i32 s8, s13, s15
	s_mov_b32 s9, m0
	s_mov_b32 m0, s8
	s_nop 0
	global_load_lds_dwordx4 v[4:5], off
	s_mov_b32 m0, s9
	v_lshl_add_u64 v[4:5], v[6:7], 0, s[4:5]
	v_readlane_b32 s16, v250, 43
	s_add_i32 s8, s13, s16
	s_mov_b32 s9, m0
	s_mov_b32 m0, s8
	s_nop 0
	global_load_lds_dwordx4 v[4:5], off
	s_mov_b32 m0, s9
	v_lshl_add_u64 v[4:5], s[6:7], 0, v[208:209]
	v_mad_u64_u32 v[6:7], s[6:7], v4, s71, v[204:205]
	v_mad_i32_i24 v7, v5, s71, v7
	v_lshl_add_u64 v[4:5], v[6:7], 0, s[86:87]
	v_lshl_add_u64 v[4:5], v[4:5], 0, s[18:19]
	s_add_i32 s6, s14, s15
	s_mov_b32 s7, m0
	s_mov_b32 m0, s6
	s_nop 0
	global_load_lds_dwordx4 v[4:5], off
	s_mov_b32 m0, s7
	v_lshl_add_u64 v[4:5], v[6:7], 0, s[4:5]
	s_add_i32 s4, s14, s16
	s_mov_b32 s5, m0
	s_mov_b32 m0, s4
	s_nop 0
	global_load_lds_dwordx4 v[4:5], off
	s_mov_b32 m0, s5
	v_or_b32_e32 v200, s0, v9
	v_mov_b64_e32 v[4:5], s[76:77]
	s_ashr_i32 s15, s11, 8
; __device__ __forceinline__ int fsw(int row) { return ((row & 3) << 2) | ((row >> 2) & 3); }
; template <int NDT>
; __device__ __forceinline__ Addr<NDT> make_addr(int kb0, int kchunk0, int vchunk0, int lane) {
;     Addr<NDT> a; const int r32 = lane & 31, hh = lane >> 5, i = lane & 15, q_ = i >> 2, p_ = i & 3, g1 = (lane >> 4) & 1;
;     const int kr = kb0 + r32, fk = fsw(kr);
; #pragma unroll
;     for (int st = 0; st < 4; ++st) a.k[st] = kr * 256 + 16 * ((kchunk0 + 2 * st + hh) ^ fk);
;     const int vr = kb0 + 4 * hh + q_, f0 = fsw(vr), f1 = fsw(vr + 8);
; #pragma unroll
;     for (int dt = 0; dt < NDT; ++dt) { const int c = vchunk0 + 4 * dt + 2 * g1 + (p_ >> 1);
;         a.v[dt][0] = 16384 + vr * 256 + 16 * (c ^ f0) + 8 * (p_ & 1); a.v[dt][1] = 16384 + (vr + 8) * 256 + 16 * (c ^ f1) + 8 * (p_ & 1); }
;     return a;
; __device__ __forceinline__ void diff_unit(int u, const f16* Z, f16* Y, const float* subln, float lam, LAS unsigned char* lds) {
;     ...
;     f16x8 qf[4];
; #pragma unroll
;     for (int st = 0; st < 4; ++st) qf[st] = *(const f16x8*)(Z + (size_t)qrow * ZP0 + 512 + 128 * h + 64 * map + 16 * st + 8 * hh);
;     asm volatile("" : "+v"(qf[0]), "+v"(qf[1]), "+v"(qf[2]), "+v"(qf[3]));
;     const Addr<4> ad = make_addr<4>(0, 8 * map, 0, lane);
;     f32x16 o[4];
; #pragma unroll
;     for (int dt = 0; dt < 4; ++dt)
; #pragma unroll
;         for (int r = 0; r < 16; ++r) o[dt][r] = 0.f;
;     float m = 0.f, l = 0.f; bool started = false;
;     f32x16 negm;
; #pragma unroll
;     for (int r = 0; r < 16; ++r) negm[r] = 0.f;
	v_mad_u64_u32 v[4:5], s[4:5], v200, s71, v[4:5]
	v_mad_i32_i24 v5, s1, v212, v5
	s_lshl_b32 s4, s15, 6
	v_bfe_u32 v6, v8, 5, 1
	v_lshl_add_u64 v[4:5], v[4:5], 0, s[86:87]
	s_ashr_i32 s5, s4, 31
	v_lshl_add_u64 v[4:5], s[4:5], 1, v[4:5]
	v_lshlrev_b32_e32 v2, 4, v6
	v_lshl_add_u64 v[4:5], v[4:5], 0, v[2:3]
	global_load_dwordx4 v[130:133], v[4:5], off offset:1120
	global_load_dwordx4 v[134:137], v[4:5], off offset:1088
	global_load_dwordx4 v[138:141], v[4:5], off offset:1056
	global_load_dwordx4 v[142:145], v[4:5], off offset:1024
	s_lshl_b32 s4, s15, 3
	v_lshlrev_b32_e32 v2, 2, v8
	v_bfe_u32 v4, v8, 2, 2
	v_lshlrev_b32_e32 v216, 2, v6
	v_lshrrev_b32_e32 v14, 3, v8
	v_and_or_b32 v2, v2, 12, v4
	v_or_b32_e32 v7, s4, v6
	v_or_b32_e32 v4, v216, v4
	v_and_b32_e32 v14, 2, v14
	v_bfe_u32 v15, v8, 1, 1
	v_and_b32_e32 v218, 63, v8
	v_lshlrev_b32_e32 v5, 8, v8
	v_bitop3_b32 v9, s4, v2, v6 bitop3:0x36
	v_bitop3_b32 v10, v7, v2, 2 bitop3:0x36
	v_bitop3_b32 v11, v7, v2, 4 bitop3:0x36
	v_bitop3_b32 v2, v7, v2, 6 bitop3:0x36
	v_and_b32_e32 v7, 12, v8
	v_or_b32_e32 v12, 8, v4
	v_or_b32_e32 v16, v14, v15
	v_lshlrev_b32_e32 v8, 3, v8
	v_lshrrev_b32_e32 v13, 2, v12
	v_and_b32_e32 v8, 8, v8
	v_or_b32_e32 v17, 4, v16
	v_and_b32_e32 v5, 0x1f00, v5
	v_lshlrev_b32_e32 v202, 3, v6
	v_or_b32_e32 v6, v6, v7
	v_bitop3_b32 v17, v13, v17, v7 bitop3:0x36
	v_or_b32_e32 v19, 8, v16
	v_or_b32_e32 v21, 12, v16
	v_lshl_add_u32 v222, v2, 4, v5
	v_lshl_or_b32 v2, v12, 8, v8
	s_lshl_b32 s2, s2, 8
	v_lshl_or_b32 v4, v4, 8, v8
	v_bitop3_b32 v14, v14, v6, v15 bitop3:0x36
	v_bitop3_b32 v15, v13, v16, v7 bitop3:0x36
	v_bitop3_b32 v18, v16, v6, 4 bitop3:0x36
	v_bitop3_b32 v20, v16, v6, 8 bitop3:0x36
	v_bitop3_b32 v19, v13, v19, v7 bitop3:0x36
	v_bitop3_b32 v6, v16, v6, 12 bitop3:0x36
	v_bitop3_b32 v7, v13, v21, v7 bitop3:0x36
	s_ashr_i32 s4, s2, 31
	v_lshl_add_u32 v226, v17, 4, v2
	v_mov_b32_e32 v16, v3
	v_mov_b32_e32 v17, v3
	v_lshl_add_u32 v219, v9, 4, v5
	v_lshl_add_u32 v220, v11, 4, v5
	v_lshl_add_u32 v221, v10, 4, v5
	s_add_u32 s16, s2, 0x8000
	v_lshl_or_b32 v223, v14, 4, v4
	v_lshl_add_u32 v224, v15, 4, v2
	v_lshl_or_b32 v225, v18, 4, v4
	v_lshl_or_b32 v227, v20, 4, v4
	v_lshl_add_u32 v228, v19, 4, v2
	v_lshl_or_b32 v229, v6, 4, v4
	v_lshl_add_u32 v230, v7, 4, v2
	v_mov_b32_e32 v2, v3
	v_mov_b32_e32 v4, v3
	v_mov_b32_e32 v5, v3
	v_mov_b32_e32 v6, v3
	v_mov_b32_e32 v7, v3
	v_mov_b32_e32 v8, v3
	v_mov_b32_e32 v9, v3
	v_mov_b32_e32 v10, v3
	v_mov_b32_e32 v11, v3
	v_mov_b32_e32 v12, v3
	v_mov_b32_e32 v13, v3
	v_mov_b32_e32 v14, v3
	v_mov_b32_e32 v15, v3
	v_mov_b32_e32 v231, 0
	v_mov_b64_e32 v[32:33], v[16:17]
	v_mov_b64_e32 v[48:49], v[16:17]
	v_mov_b64_e32 v[64:65], v[16:17]
	v_mov_b64_e32 v[80:81], v[16:17]
	v_mov_b32_e32 v201, s1
	s_addc_u32 s17, s4, 0
	s_mov_b32 s18, 0
	s_mov_b64 s[4:5], 0
	s_mov_b32 s19, 0x18000
	s_movk_i32 s20, 0xc0
	s_lshl_b32 s2, s3, 1
	v_mov_b64_e32 v[30:31], v[14:15]
	v_mov_b64_e32 v[28:29], v[12:13]
	v_mov_b64_e32 v[26:27], v[10:11]
	v_mov_b64_e32 v[24:25], v[8:9]
	v_mov_b64_e32 v[22:23], v[6:7]
	v_mov_b64_e32 v[20:21], v[4:5]
	v_mov_b64_e32 v[18:19], v[2:3]
	v_mov_b64_e32 v[46:47], v[14:15]
	v_mov_b64_e32 v[44:45], v[12:13]
	v_mov_b64_e32 v[42:43], v[10:11]
	v_mov_b64_e32 v[40:41], v[8:9]
	v_mov_b64_e32 v[38:39], v[6:7]
	v_mov_b64_e32 v[36:37], v[4:5]
	v_mov_b64_e32 v[34:35], v[2:3]
	v_mov_b64_e32 v[62:63], v[14:15]
	v_mov_b64_e32 v[60:61], v[12:13]
	v_mov_b64_e32 v[58:59], v[10:11]
	v_mov_b64_e32 v[56:57], v[8:9]
	v_mov_b64_e32 v[54:55], v[6:7]
	v_mov_b64_e32 v[52:53], v[4:5]
	v_mov_b64_e32 v[50:51], v[2:3]
	v_mov_b32_e32 v232, 0
	v_mov_b64_e32 v[78:79], v[14:15]
	v_mov_b64_e32 v[76:77], v[12:13]
	v_mov_b64_e32 v[74:75], v[10:11]
	v_mov_b64_e32 v[72:73], v[8:9]
	v_mov_b64_e32 v[70:71], v[6:7]
	v_mov_b64_e32 v[68:69], v[4:5]
	v_mov_b64_e32 v[66:67], v[2:3]
	v_mov_b32_e32 v82, 0
	v_mov_b32_e32 v83, v231
	v_mov_b32_e32 v84, v231
	v_mov_b32_e32 v85, v231
	v_mov_b32_e32 v86, v231
	v_mov_b32_e32 v87, v231
	v_mov_b32_e32 v88, v231
	v_mov_b32_e32 v89, v231
	v_mov_b32_e32 v90, v231
	v_mov_b32_e32 v91, v231
	v_mov_b32_e32 v92, v231
	v_mov_b32_e32 v93, v231
	v_mov_b32_e32 v94, v231
	v_mov_b32_e32 v95, v231
	v_mov_b32_e32 v96, v231
	v_mov_b32_e32 v97, v231
	s_waitcnt vmcnt(0)
	s_cmp_eq_u32 s98, 0
	s_cbranch_scc1 .Lmy_d1
	s_barrier

;     if (__any(d != 0.f)) {
; #pragma unroll
;         for (int r = 0; r < 16; ++r) s[r] -= d; }
; #pragma unroll
;     for (int r = 0; r < 16; ++r) { s[r] = __builtin_amdgcn_exp2f(s[r]); ps += s[r]; }
;     return ps; }
; template <int NDT>
; __device__ __forceinline__ void step64(LAS unsigned char* slot, const Addr<NDT>& a, const f16x8 (&qf)[4], f32x16 (&o)[NDT], float& m, float& l, f32x16& negm, bool& started) {
;     ...
;     float mx = fmaxf(rowmax16(s0), rowmax16(s1)); mx = fmaxf(mx, __shfl_xor(mx, 32));
;     const float d = rescale<NDT>(mx, m, l, o, negm, started);
;     l += expsum(s0, d) + expsum(s1, d);
.LBB0_549:
	v_exp_f32_e32 v2, v114
	v_exp_f32_e32 v244, v98
	v_exp_f32_e32 v233, v115
	v_exp_f32_e32 v245, v99
	v_exp_f32_e32 v242, v116
	v_exp_f32_e32 v246, v100
	v_exp_f32_e32 v243, v117
	v_exp_f32_e32 v247, v101
	v_add_f32_e32 v16, 0, v2
	v_exp_f32_e32 v114, v118
	v_add_f32_e32 v17, 0, v244
	v_exp_f32_e32 v115, v102
	v_add_f32_e32 v16, v233, v16
	v_exp_f32_e32 v116, v119
	v_add_f32_e32 v17, v245, v17
	v_exp_f32_e32 v117, v103
	v_add_f32_e32 v16, v242, v16
	v_exp_f32_e32 v118, v120
	v_add_f32_e32 v17, v246, v17
	v_exp_f32_e32 v119, v104
	v_add_f32_e32 v16, v243, v16
	v_exp_f32_e32 v120, v121
	v_add_f32_e32 v17, v247, v17
	v_exp_f32_e32 v121, v105
	v_exp_f32_e32 v122, v122
	v_exp_f32_e32 v234, v123
	v_exp_f32_e32 v123, v106
	v_pk_add_f32 v[16:17], v[114:115], v[16:17]
	v_exp_f32_e32 v235, v107
	v_pk_add_f32 v[16:17], v[116:117], v[16:17]
	v_exp_f32_e32 v124, v124
	v_exp_f32_e32 v236, v125
	v_exp_f32_e32 v125, v108
	v_pk_add_f32 v[16:17], v[118:119], v[16:17]
	v_exp_f32_e32 v237, v109
	v_pk_add_f32 v[16:17], v[120:121], v[16:17]
	v_exp_f32_e32 v126, v126
	v_exp_f32_e32 v238, v127
	v_exp_f32_e32 v127, v110
	v_pk_add_f32 v[16:17], v[122:123], v[16:17]
	v_exp_f32_e32 v239, v111
	v_pk_add_f32 v[16:17], v[234:235], v[16:17]
	v_exp_f32_e32 v128, v128
	v_exp_f32_e32 v240, v129
	v_exp_f32_e32 v129, v112
	v_pk_add_f32 v[16:17], v[124:125], v[16:17]
	v_exp_f32_e32 v241, v113
	v_pk_add_f32 v[16:17], v[236:237], v[16:17]
	s_nop 0
	v_pk_add_f32 v[16:17], v[126:127], v[16:17]
	s_nop 0
	v_pk_add_f32 v[16:17], v[238:239], v[16:17]
	s_nop 0
	v_pk_add_f32 v[16:17], v[128:129], v[16:17]
	s_nop 0
	v_pk_add_f32 v[16:17], v[240:241], v[16:17]
	s_nop 0
	v_add_f32_e32 v16, v16, v17
	v_add_f32_e32 v231, v231, v16
	s_cmp_gt_u32 s18, 32
	s_cbranch_scc1 .Lmy_d2
	s_waitcnt vmcnt(8)
	s_branch .Lmy_d3

; __device__ __forceinline__ void wait_tile(int younger) { if (younger >= 2) AT_WAIT(8); else if (younger == 1) AT_WAIT(4); else AT_WAIT(0); }
; template <int NDT>
; __device__ __forceinline__ void pv32(const f16x8* vf, const f32x16& p, f32x16 (&o)[NDT]) {
; #pragma unroll
;     for (int s2 = 0; s2 < 2; ++s2) {
;         f16x8 pb;
; #pragma unroll
;         for (int j = 0; j < 8; ++j) pb[j] = (f16)p[8 * s2 + j];
; #pragma unroll
;         for (int dt = 0; dt < NDT; ++dt) o[dt] = __builtin_amdgcn_mfma_f32_32x32x16_f16(vf[s2 * NDT + dt], pb, o[dt], 0, 0, 0);
;     }
; }
; __device__ __forceinline__ void diff_unit(int u, const f16* Z, f16* Y, const float* subln, float lam, LAS unsigned char* lds) {
;     ...
;     for (int t = 0; t < NT; ++t) {
;         wait_tile(NT - 1 - t);
;         __builtin_amdgcn_s_barrier();
;         if (t + 3 < NT) dma_tile(Z, DIFF_ROWBASE(t + 3), kcol, vcol, lds + ((t + 3) & 3) * SLOT, wave, lane);
;         step64<4>(lds + (t & 3) * SLOT, ad, qf, o, m, l, negm, started);
;     }
.Lmy_d3:
	s_barrier
	v_cvt_pk_f16_f32 v101, v118, v120
	v_cvt_pk_f16_f32 v100, v114, v116
	v_cvt_pk_f16_f32 v99, v242, v243
	v_cvt_pk_f16_f32 v98, v2, v233
	s_nop 1
	v_mfma_f32_32x32x16_f16 v[66:81], v[154:157], v[98:101], v[66:81]
	v_mfma_f32_32x32x16_f16 v[50:65], v[166:169], v[98:101], v[50:65]
	v_mfma_f32_32x32x16_f16 v[34:49], v[174:177], v[98:101], v[34:49]
	v_mfma_f32_32x32x16_f16 v[18:33], v[178:181], v[98:101], v[18:33]
	v_cvt_pk_f16_f32 v101, v128, v240
	v_cvt_pk_f16_f32 v100, v126, v238
	v_cvt_pk_f16_f32 v99, v124, v236
	v_cvt_pk_f16_f32 v98, v122, v234
	s_nop 1
	v_mfma_f32_32x32x16_f16 v[66:81], v[4:7], v[98:101], v[66:81]
	v_cvt_pk_f16_f32 v7, v119, v121
	v_cvt_pk_f16_f32 v6, v115, v117
	v_cvt_pk_f16_f32 v5, v246, v247
	v_cvt_pk_f16_f32 v4, v244, v245
	v_mfma_f32_32x32x16_f16 v[50:65], v[8:11], v[98:101], v[50:65]
	v_mfma_f32_32x32x16_f16 v[34:49], v[12:15], v[98:101], v[34:49]
	v_mfma_f32_32x32x16_f16 v[18:33], v[146:149], v[98:101], v[18:33]
	v_mfma_f32_32x32x16_f16 v[66:81], v[170:173], v[4:7], v[66:81]
	v_mfma_f32_32x32x16_f16 v[50:65], v[182:185], v[4:7], v[50:65]
	v_mfma_f32_32x32x16_f16 v[34:49], v[186:189], v[4:7], v[34:49]
	v_mfma_f32_32x32x16_f16 v[18:33], v[194:197], v[4:7], v[18:33]
	v_cvt_pk_f16_f32 v7, v129, v241
	v_cvt_pk_f16_f32 v6, v127, v239
	v_cvt_pk_f16_f32 v5, v125, v237
	v_cvt_pk_f16_f32 v4, v123, v235
	s_nop 1
	v_mfma_f32_32x32x16_f16 v[66:81], v[150:153], v[4:7], v[66:81]
	v_mfma_f32_32x32x16_f16 v[50:65], v[158:161], v[4:7], v[50:65]
	v_mfma_f32_32x32x16_f16 v[34:49], v[162:165], v[4:7], v[34:49]
	v_mfma_f32_32x32x16_f16 v[18:33], v[190:193], v[4:7], v[18:33]
	s_add_i32 s18, s18, 1
	s_add_i32 s19, s19, 0x8000
	s_add_i32 s20, s20, 64
	s_cmp_eq_u32 s19, 0x138000
	s_cbranch_scc1 .LBB0_572

; __device__ __forceinline__ void wait_tile(int younger) { if (younger >= 2) AT_WAIT(8); else if (younger == 1) AT_WAIT(4); else AT_WAIT(0); }
; __device__ __forceinline__ void diff_unit(int u, const f16* Z, f16* Y, const float* subln, float lam, LAS unsigned char* lds) {
;     ...
;     for (int t = 0; t < NT; ++t) {
;         wait_tile(NT - 1 - t);
;         __builtin_amdgcn_s_barrier();
;         if (t + 3 < NT) dma_tile(Z, DIFF_ROWBASE(t + 3), kcol, vcol, lds + ((t + 3) & 3) * SLOT, wave, lane);
;         step64<4>(lds + (t & 3) * SLOT, ad, qf, o, m, l, negm, started);
;     }
;     ...
;     __syncthreads();
.LBB0_572:
	s_cmp_lg_u32 s98, 0
	s_cbranch_scc1 .Lmy_d4
	s_barrier

; #define LAS __attribute__((address_space(3)))
; __global__ void __launch_bounds__(512, 2) fwd(Params p) {
;     extern __shared__ __attribute__((aligned(16))) unsigned char lds_raw[];
;     LAS unsigned char* lds = (LAS unsigned char*)lds_raw;
	.amdhsa_kernel _Z3fwd6Params
		.amdhsa_group_segment_fixed_size 0
		.amdhsa_private_segment_fixed_size 0
		.amdhsa_kernarg_size 576
		.amdhsa_user_sgpr_count 2
		.amdhsa_user_sgpr_dispatch_ptr 0
		.amdhsa_user_sgpr_queue_ptr 0
		.amdhsa_user_sgpr_kernarg_segment_ptr 1
		.amdhsa_user_sgpr_dispatch_id 0
		.amdhsa_user_sgpr_kernarg_preload_length 0
		.amdhsa_user_sgpr_kernarg_preload_offset 0
		.amdhsa_user_sgpr_private_segment_size 0
		.amdhsa_uses_dynamic_stack 0
		.amdhsa_enable_private_segment 0
		.amdhsa_system_sgpr_workgroup_id_x 1
		.amdhsa_system_sgpr_workgroup_id_y 0
		.amdhsa_system_sgpr_workgroup_id_z 0
		.amdhsa_system_sgpr_workgroup_info 0
		.amdhsa_system_vgpr_workitem_id 0
		.amdhsa_next_free_vgpr 252
		.amdhsa_next_free_sgpr 100
		.amdhsa_accum_offset 252
		.amdhsa_reserve_vcc 1
		.amdhsa_float_round_mode_32 0
		.amdhsa_float_round_mode_16_64 0
		.amdhsa_float_denorm_mode_32 3
		.amdhsa_float_denorm_mode_16_64 3
		.amdhsa_dx10_clamp 1
		.amdhsa_ieee_mode 1
		.amdhsa_fp16_overflow 0
		.amdhsa_tg_split 0
		.amdhsa_exception_fp_ieee_invalid_op 0
		.amdhsa_exception_fp_denorm_src 0
		.amdhsa_exception_fp_ieee_div_zero 0
		.amdhsa_exception_fp_ieee_overflow 0
		.amdhsa_exception_fp_ieee_underflow 0
		.amdhsa_exception_fp_ieee_inexact 0
		.amdhsa_exception_int_div_zero 0
	.end_amdhsa_kernel

; #define LAS __attribute__((address_space(3)))
; __global__ void __launch_bounds__(512, 2) fwd(Params p) {
;     extern __shared__ __attribute__((aligned(16))) unsigned char lds_raw[];
;     LAS unsigned char* lds = (LAS unsigned char*)lds_raw;
amdhsa.kernels:
  - .agpr_count:     0
    .args:
      - .offset:         0
        .size:           320
        .value_kind:     by_value
      - .offset:         320
        .size:           4
        .value_kind:     hidden_block_count_x
      - .offset:         324
        .size:           4
        .value_kind:     hidden_block_count_y
      - .offset:         328
        .size:           4
        .value_kind:     hidden_block_count_z
      - .offset:         332
        .size:           2
        .value_kind:     hidden_group_size_x
      - .offset:         334
        .size:           2
        .value_kind:     hidden_group_size_y
      - .offset:         336
        .size:           2
        .value_kind:     hidden_group_size_z
      - .offset:         338
        .size:           2
        .value_kind:     hidden_remainder_x
      - .offset:         340
        .size:           2
        .value_kind:     hidden_remainder_y
      - .offset:         342
        .size:           2
        .value_kind:     hidden_remainder_z
      - .offset:         360
        .size:           8
        .value_kind:     hidden_global_offset_x
      - .offset:         368
        .size:           8
        .value_kind:     hidden_global_offset_y
      - .offset:         376
        .size:           8
        .value_kind:     hidden_global_offset_z
      - .offset:         384
        .size:           2
        .value_kind:     hidden_grid_dims
      - .offset:         440
        .size:           4
        .value_kind:     hidden_dynamic_lds_size
    .group_segment_fixed_size: 0
    .kernarg_segment_align: 8
    .kernarg_segment_size: 576
    .language:       OpenCL C
    .language_version:
      - 2
      - 0
    .max_flat_workgroup_size: 512
    .name:           _Z3fwd6Params
    .private_segment_fixed_size: 0
    .sgpr_count:     106
    .sgpr_spill_count: 133
    .symbol:         _Z3fwd6Params.kd
    .uniform_work_group_size: 1
    .uses_dynamic_stack: false
    .vgpr_count:     252
    .vgpr_spill_count: 0
    .wavefront_size: 64
